# v69 + GEMM phase prologue de-serialised: all 14 staging pieces issued before the first counted wait (7 sites)
# baseline (speedup 1.0000x reference)
.LBB0_281:
	v_lshl_add_u64 v[10:11], s[22:23], 0, v[34:35]
	v_mov_b32_e32 v165, v35
	v_readlane_b32 s30, v253, 46
	v_bfe_u32 v189, v4, 4, 2
	s_lshl_b32 s5, s5, 5
	v_lshl_add_u64 v[12:13], s[22:23], 0, v[164:165]
	v_mov_b32_e32 v169, v35
	v_readlane_b32 s31, v253, 47
	v_and_b32_e32 v1, 15, v4
	v_lshlrev_b32_e32 v9, 4, v189
	v_lshlrev_b32_e32 v4, 2, v4
	s_and_b32 s46, s5, 0x60
	s_add_i32 m0, s41, 0x18000
	v_lshl_add_u64 v[10:11], v[10:11], 0, s[18:19]
	v_lshl_add_u64 v[14:15], s[30:31], 0, v[168:169]
	v_mov_b32_e32 v167, v35
	s_lshl_b32 s45, s8, 6
	v_lshl_or_b32 v9, v1, 6, v9
	s_lshl_b32 s8, s8, 13
	v_and_b32_e32 v4, 32, v4
	s_lshl_b32 s5, s46, 7
	global_load_lds_dwordx4 v[10:11], off
	v_lshl_add_u64 v[10:11], v[12:13], 0, s[18:19]
	s_add_i32 m0, s41, 0x1a000
	s_add_i32 s47, s41, 0x8000
	s_add_i32 s48, s41, 0xa000
	v_lshl_add_u64 v[16:17], s[30:31], 0, v[166:167]
	v_bitop3_b32 v18, v9, s8, v4 bitop3:0xde
	global_load_lds_dwordx4 v[10:11], off
	v_lshl_add_u64 v[10:11], v[14:15], 0, s[18:19]
	s_mov_b32 m0, s47
	s_add_u32 s8, s22, 0x40080
	global_load_lds_dwordx4 v[10:11], off
	v_lshl_add_u64 v[10:11], v[16:17], 0, s[18:19]
	s_mov_b32 m0, s48
	s_addc_u32 s9, s23, 0
	global_load_lds_dwordx4 v[10:11], off
	s_add_i32 m0, s41, 0x1c000
	v_lshl_add_u64 v[10:11], s[8:9], 0, v[34:35]
	global_load_lds_dwordx4 v[10:11], off
	v_lshl_add_u64 v[10:11], s[8:9], 0, v[164:165]
	s_add_i32 m0, s41, 0x1e000
	v_bitop3_b32 v196, v9, s5, v4 bitop3:0xde
	global_load_lds_dwordx4 v[10:11], off
	v_lshlrev_b32_e32 v4, 14, v7
	v_and_b32_e32 v4, 0xffff8000, v4
	v_lshl_add_u32 v4, v6, 11, v4
	v_and_b32_e32 v6, 1, v7
	v_lshl_or_b32 v4, v6, 6, v4
	v_lshl_add_u32 v170, v8, 1, v4
	v_lshlrev_b32_e32 v4, 14, v2
	v_and_b32_e32 v4, 0xffff8000, v4
	v_lshl_add_u32 v3, v3, 11, v4
	v_and_b32_e32 v2, 1, v2
	s_waitcnt vmcnt(8)
	s_barrier
	s_waitcnt vmcnt(6)
	v_lshl_or_b32 v2, v2, 6, v3
	s_cmpk_lt_u32 s4, 0x100
	v_lshl_add_u32 v172, v5, 1, v2
	v_mov_b32_e32 v2, 0
	s_cselect_b64 s[8:9], -1, 0
	v_mov_b32_e32 v171, v35
	v_mov_b32_e32 v173, v35
	s_mov_b32 s49, 0
	v_add_u32_e32 v197, 0, v18
	v_readlane_b32 s52, v253, 44
	v_readlane_b32 s53, v253, 43
	v_mov_b32_e32 v3, v2
	v_mov_b32_e32 v4, v2
	v_mov_b32_e32 v5, v2
	v_mov_b32_e32 v6, v2
	v_mov_b32_e32 v7, v2
	v_mov_b32_e32 v8, v2
	v_mov_b32_e32 v9, v2
	v_mov_b32_e32 v10, v2
	v_mov_b32_e32 v11, v2
	v_mov_b32_e32 v12, v2
	v_mov_b32_e32 v13, v2
	v_mov_b32_e32 v14, v2
	v_mov_b32_e32 v15, v2
	v_mov_b32_e32 v16, v2
	v_mov_b32_e32 v17, v2
	v_mov_b32_e32 v18, v2
	v_mov_b32_e32 v19, v2
	v_mov_b32_e32 v20, v2
	v_mov_b32_e32 v21, v2
	v_mov_b32_e32 v22, v2
	v_mov_b32_e32 v23, v2
	v_mov_b32_e32 v24, v2
	v_mov_b32_e32 v25, v2
	v_mov_b32_e32 v26, v2
	v_mov_b32_e32 v27, v2
	v_mov_b32_e32 v28, v2
	v_mov_b32_e32 v29, v2
	v_mov_b32_e32 v30, v2
	v_mov_b32_e32 v31, v2
	v_mov_b32_e32 v32, v2
	v_mov_b32_e32 v33, v2
	v_mov_b32_e32 v36, v2
	v_mov_b32_e32 v37, v2
	v_mov_b32_e32 v38, v2
	v_mov_b32_e32 v39, v2
	v_mov_b32_e32 v40, v2
	v_mov_b32_e32 v41, v2
	v_mov_b32_e32 v42, v2
	v_mov_b32_e32 v43, v2
	v_mov_b32_e32 v44, v2
	v_mov_b32_e32 v45, v2
	v_mov_b32_e32 v46, v2
	v_mov_b32_e32 v47, v2
	v_mov_b32_e32 v48, v2
	v_mov_b32_e32 v49, v2
	v_mov_b32_e32 v50, v2
	v_mov_b32_e32 v51, v2
	v_mov_b32_e32 v52, v2
	v_mov_b32_e32 v53, v2
	v_mov_b32_e32 v54, v2
	v_mov_b32_e32 v55, v2
	v_mov_b32_e32 v56, v2
	v_mov_b32_e32 v57, v2
	v_mov_b32_e32 v58, v2
	v_mov_b32_e32 v59, v2
	v_mov_b32_e32 v60, v2
	v_mov_b32_e32 v61, v2
	v_mov_b32_e32 v62, v2
	v_mov_b32_e32 v63, v2
	v_mov_b32_e32 v64, v2
	v_mov_b32_e32 v65, v2
	v_mov_b32_e32 v66, v2
	v_mov_b32_e32 v67, v2
	v_mov_b32_e32 v68, v2
	v_mov_b32_e32 v69, v2
	v_mov_b32_e32 v70, v2
	v_mov_b32_e32 v71, v2
	v_mov_b32_e32 v72, v2
	v_mov_b32_e32 v73, v2
	v_mov_b32_e32 v74, v2
	v_mov_b32_e32 v75, v2
	v_mov_b32_e32 v76, v2
	v_mov_b32_e32 v77, v2
	v_mov_b32_e32 v78, v2
	v_mov_b32_e32 v79, v2
	v_mov_b32_e32 v80, v2
	v_mov_b32_e32 v81, v2
	v_mov_b32_e32 v82, v2
	v_mov_b32_e32 v83, v2
	v_mov_b32_e32 v84, v2
	v_mov_b32_e32 v85, v2
	v_mov_b32_e32 v86, v2
	v_mov_b32_e32 v87, v2
	v_mov_b32_e32 v88, v2
	v_mov_b32_e32 v89, v2
	v_mov_b32_e32 v90, v2
	v_mov_b32_e32 v91, v2
	v_mov_b32_e32 v92, v2
	v_mov_b32_e32 v93, v2
	v_mov_b32_e32 v94, v2
	v_mov_b32_e32 v95, v2
	v_mov_b32_e32 v96, v2
	v_mov_b32_e32 v97, v2
	v_mov_b32_e32 v98, v2
	v_mov_b32_e32 v99, v2
	v_mov_b32_e32 v100, v2
	v_mov_b32_e32 v101, v2
	v_mov_b32_e32 v102, v2
	v_mov_b32_e32 v103, v2
	v_mov_b32_e32 v104, v2
	v_mov_b32_e32 v105, v2
	v_mov_b32_e32 v106, v2
	v_mov_b32_e32 v107, v2
	v_mov_b32_e32 v108, v2
	v_mov_b32_e32 v109, v2
	v_mov_b32_e32 v110, v2
	v_mov_b32_e32 v111, v2
	v_mov_b32_e32 v112, v2
	v_mov_b32_e32 v113, v2
	v_mov_b32_e32 v114, v2
	v_mov_b32_e32 v115, v2
	v_mov_b32_e32 v116, v2
	v_mov_b32_e32 v117, v2
	v_mov_b32_e32 v118, v2
	v_mov_b32_e32 v119, v2
	v_mov_b32_e32 v120, v2
	v_mov_b32_e32 v121, v2
	v_mov_b32_e32 v122, v2
	v_mov_b32_e32 v123, v2
	v_mov_b32_e32 v124, v2
	v_mov_b32_e32 v125, v2
	v_mov_b32_e32 v126, v2
	v_mov_b32_e32 v127, v2
	v_mov_b32_e32 v128, v2
	v_mov_b32_e32 v129, v2
	v_mov_b32_e32 v130, v2
	v_mov_b32_e32 v131, v2
	s_barrier
	s_branch .LBB0_284

.LBB0_531:
	v_readlane_b32 s8, v255, 17
	v_readlane_b32 s9, v255, 18
	s_cmp_eq_u32 s8, 3
	v_readlane_b32 s8, v252, 5
	s_cselect_b32 s9, s8, s81
	v_readlane_b32 s8, v252, 4
	v_readlane_b32 s11, v255, 11
	s_cselect_b32 s8, s8, s80
	s_add_u32 s47, s11, 0x2000
	v_readlane_b32 s11, v255, 12
	v_readlane_b32 s36, v253, 55
	s_addc_u32 s48, s11, 0
	v_bfe_u32 v189, v8, 4, 2
	s_lshl_b32 s5, s5, 5
	v_mov_b32_e32 v195, v35
	v_readlane_b32 s37, v253, 56
	v_and_b32_e32 v1, 15, v8
	v_lshlrev_b32_e32 v13, 4, v189
	v_lshlrev_b32_e32 v8, 2, v8
	s_and_b32 s50, s5, 0x60
	s_add_i32 m0, s43, 0x18000
	v_lshl_add_u64 v[2:3], v[2:3], 0, s[18:19]
	v_lshl_add_u64 v[14:15], s[36:37], 0, v[194:195]
	v_mov_b32_e32 v193, v35
	s_lshl_b32 s49, s10, 6
	v_lshl_or_b32 v13, v1, 6, v13
	s_lshl_b32 s10, s10, 13
	v_and_b32_e32 v8, 32, v8
	s_lshl_b32 s5, s50, 7
	global_load_lds_dwordx4 v[2:3], off
	v_lshl_add_u64 v[2:3], v[4:5], 0, s[18:19]
	s_add_i32 m0, s43, 0x1a000
	s_add_i32 s51, s43, 0x8000
	s_add_i32 s52, s43, 0xa000
	v_lshl_add_u64 v[16:17], s[36:37], 0, v[192:193]
	v_bitop3_b32 v18, v13, s10, v8 bitop3:0xde
	global_load_lds_dwordx4 v[2:3], off
	v_lshl_add_u64 v[2:3], v[14:15], 0, s[18:19]
	s_mov_b32 m0, s51
	s_add_u32 s10, s30, 0x40080
	global_load_lds_dwordx4 v[2:3], off
	v_lshl_add_u64 v[2:3], v[16:17], 0, s[18:19]
	s_mov_b32 m0, s52
	s_addc_u32 s11, s31, 0
	global_load_lds_dwordx4 v[2:3], off
	s_add_i32 m0, s43, 0x1c000
	v_lshl_add_u64 v[2:3], s[10:11], 0, v[34:35]
	global_load_lds_dwordx4 v[2:3], off
	v_lshl_add_u64 v[2:3], s[10:11], 0, v[190:191]
	s_add_i32 m0, s43, 0x1e000
	s_cmpk_lt_u32 s4, 0x100
	global_load_lds_dwordx4 v[2:3], off
	v_lshlrev_b32_e32 v2, 14, v11
	v_and_b32_e32 v2, 0xffff8000, v2
	v_lshl_add_u32 v2, v10, 11, v2
	v_and_b32_e32 v3, 1, v11
	v_lshl_or_b32 v2, v3, 6, v2
	v_lshl_add_u32 v196, v12, 1, v2
	v_lshlrev_b32_e32 v2, 14, v6
	v_and_b32_e32 v2, 0xffff8000, v2
	v_lshl_add_u32 v2, v7, 11, v2
	v_and_b32_e32 v3, 1, v6
	s_waitcnt vmcnt(8)
	s_barrier
	s_waitcnt vmcnt(6)
	v_lshl_or_b32 v2, v3, 6, v2
	v_lshl_add_u32 v198, v9, 1, v2
	v_mov_b32_e32 v2, 0
	v_bitop3_b32 v222, v13, s5, v8 bitop3:0xde
	s_cselect_b64 s[10:11], -1, 0
	v_mov_b32_e32 v197, v35
	v_mov_b32_e32 v199, v35
	s_mov_b32 s53, 0
	v_add_u32_e32 v223, 0, v18
	v_readlane_b32 s57, v253, 51
	v_readlane_b32 s56, v253, 50
	v_mov_b32_e32 v3, v2
	v_mov_b32_e32 v4, v2
	v_mov_b32_e32 v5, v2
	v_mov_b32_e32 v6, v2
	v_mov_b32_e32 v7, v2
	v_mov_b32_e32 v8, v2
	v_mov_b32_e32 v9, v2
	v_mov_b32_e32 v10, v2
	v_mov_b32_e32 v11, v2
	v_mov_b32_e32 v12, v2
	v_mov_b32_e32 v13, v2
	v_mov_b32_e32 v14, v2
	v_mov_b32_e32 v15, v2
	v_mov_b32_e32 v16, v2
	v_mov_b32_e32 v17, v2
	v_mov_b32_e32 v18, v2
	v_mov_b32_e32 v19, v2
	v_mov_b32_e32 v20, v2
	v_mov_b32_e32 v21, v2
	v_mov_b32_e32 v22, v2
	v_mov_b32_e32 v23, v2
	v_mov_b32_e32 v24, v2
	v_mov_b32_e32 v25, v2
	v_mov_b32_e32 v26, v2
	v_mov_b32_e32 v27, v2
	v_mov_b32_e32 v28, v2
	v_mov_b32_e32 v29, v2
	v_mov_b32_e32 v30, v2
	v_mov_b32_e32 v31, v2
	v_mov_b32_e32 v32, v2
	v_mov_b32_e32 v33, v2
	v_mov_b32_e32 v36, v2
	v_mov_b32_e32 v37, v2
	v_mov_b32_e32 v38, v2
	v_mov_b32_e32 v39, v2
	v_mov_b32_e32 v40, v2
	v_mov_b32_e32 v41, v2
	v_mov_b32_e32 v42, v2
	v_mov_b32_e32 v43, v2
	v_mov_b32_e32 v44, v2
	v_mov_b32_e32 v45, v2
	v_mov_b32_e32 v46, v2
	v_mov_b32_e32 v47, v2
	v_mov_b32_e32 v48, v2
	v_mov_b32_e32 v49, v2
	v_mov_b32_e32 v50, v2
	v_mov_b32_e32 v51, v2
	v_mov_b32_e32 v52, v2
	v_mov_b32_e32 v53, v2
	v_mov_b32_e32 v54, v2
	v_mov_b32_e32 v55, v2
	v_mov_b32_e32 v56, v2
	v_mov_b32_e32 v57, v2
	v_mov_b32_e32 v58, v2
	v_mov_b32_e32 v59, v2
	v_mov_b32_e32 v60, v2
	v_mov_b32_e32 v61, v2
	v_mov_b32_e32 v62, v2
	v_mov_b32_e32 v63, v2
	v_mov_b32_e32 v64, v2
	v_mov_b32_e32 v65, v2
	v_mov_b32_e32 v66, v2
	v_mov_b32_e32 v67, v2
	v_mov_b32_e32 v68, v2
	v_mov_b32_e32 v69, v2
	v_mov_b32_e32 v70, v2
	v_mov_b32_e32 v71, v2
	v_mov_b32_e32 v72, v2
	v_mov_b32_e32 v73, v2
	v_mov_b32_e32 v74, v2
	v_mov_b32_e32 v75, v2
	v_mov_b32_e32 v76, v2
	v_mov_b32_e32 v77, v2
	v_mov_b32_e32 v78, v2
	v_mov_b32_e32 v79, v2
	v_mov_b32_e32 v80, v2
	v_mov_b32_e32 v81, v2
	v_mov_b32_e32 v82, v2
	v_mov_b32_e32 v83, v2
	v_mov_b32_e32 v84, v2
	v_mov_b32_e32 v85, v2
	v_mov_b32_e32 v86, v2
	v_mov_b32_e32 v87, v2
	v_mov_b32_e32 v88, v2
	v_mov_b32_e32 v89, v2
	v_mov_b32_e32 v90, v2
	v_mov_b32_e32 v91, v2
	v_mov_b32_e32 v92, v2
	v_mov_b32_e32 v93, v2
	v_mov_b32_e32 v94, v2
	v_mov_b32_e32 v95, v2
	v_mov_b32_e32 v96, v2
	v_mov_b32_e32 v97, v2
	v_mov_b32_e32 v98, v2
	v_mov_b32_e32 v99, v2
	v_mov_b32_e32 v100, v2
	v_mov_b32_e32 v101, v2
	v_mov_b32_e32 v102, v2
	v_mov_b32_e32 v103, v2
	v_mov_b32_e32 v104, v2
	v_mov_b32_e32 v105, v2
	v_mov_b32_e32 v106, v2
	v_mov_b32_e32 v107, v2
	v_mov_b32_e32 v108, v2
	v_mov_b32_e32 v109, v2
	v_mov_b32_e32 v110, v2
	v_mov_b32_e32 v111, v2
	v_mov_b32_e32 v112, v2
	v_mov_b32_e32 v113, v2
	v_mov_b32_e32 v114, v2
	v_mov_b32_e32 v115, v2
	v_mov_b32_e32 v116, v2
	v_mov_b32_e32 v117, v2
	v_mov_b32_e32 v118, v2
	v_mov_b32_e32 v119, v2
	v_mov_b32_e32 v120, v2
	v_mov_b32_e32 v121, v2
	v_mov_b32_e32 v122, v2
	v_mov_b32_e32 v123, v2
	v_mov_b32_e32 v124, v2
	v_mov_b32_e32 v125, v2
	v_mov_b32_e32 v126, v2
	v_mov_b32_e32 v127, v2
	v_mov_b32_e32 v128, v2
	v_mov_b32_e32 v129, v2
	v_mov_b32_e32 v130, v2
	v_mov_b32_e32 v131, v2
	s_barrier
	s_branch .LBB0_534

.LBB0_809:
	v_bfe_u32 v165, v168, 4, 2
	v_and_b32_e32 v1, 15, v168
	v_lshlrev_b32_e32 v6, 4, v165
	v_lshlrev_b32_e32 v7, 2, v168
	s_lshl_b32 s73, s4, 6
	v_lshl_or_b32 v6, v1, 6, v6
	s_lshl_b32 s4, s4, 13
	v_and_b32_e32 v7, 32, v7
	v_bitop3_b32 v8, v6, s4, v7 bitop3:0xde
	s_lshl_b32 s4, s5, 5
	v_mov_b32_e32 v171, v35
	s_and_b32 s74, s4, 0x60
	v_lshl_add_u64 v[2:3], s[30:31], 0, v[170:171]
	v_mov_b32_e32 v173, v35
	s_lshl_b32 s4, s74, 7
	v_lshl_add_u64 v[4:5], s[30:31], 0, v[172:173]
	v_bitop3_b32 v167, v6, s4, v7 bitop3:0xde
	s_add_i32 m0, s69, 0x18000
	v_lshl_add_u64 v[2:3], v[2:3], 0, s[18:19]
	v_readlane_b32 s4, v253, 28
	global_load_lds_dwordx4 v[2:3], off
	v_lshl_add_u64 v[2:3], v[4:5], 0, s[18:19]
	s_add_i32 m0, s69, 0x1a000
	v_readlane_b32 s5, v253, 29
	s_add_i32 s75, s69, 0x8000
	v_mov_b32_e32 v193, v35
	global_load_lds_dwordx4 v[2:3], off
	v_lshl_add_u64 v[2:3], s[4:5], 0, v[34:35]
	s_mov_b32 m0, s75
	s_add_i32 s76, s69, 0xa000
	global_load_lds_dwordx4 v[2:3], off
	v_lshl_add_u64 v[2:3], s[4:5], 0, v[192:193]
	s_add_u32 s4, s30, 0x20080
	s_mov_b32 m0, s76
	s_addc_u32 s5, s31, 0
	global_load_lds_dwordx4 v[2:3], off
	s_add_i32 m0, s69, 0x1c000
	v_lshl_add_u64 v[2:3], s[4:5], 0, v[170:171]
	global_load_lds_dwordx4 v[2:3], off
	v_lshl_add_u64 v[2:3], s[4:5], 0, v[172:173]
	s_add_i32 m0, s69, 0x1e000
	v_mov_b32_e32 v36, 0
	global_load_lds_dwordx4 v[2:3], off
	s_waitcnt vmcnt(8)
	s_barrier
	s_waitcnt vmcnt(6)
	s_cmpk_lt_u32 s16, 0x100
	s_mov_b32 s77, 0
	s_cselect_b64 s[16:17], -1, 0
	v_add_u32_e32 v169, 0, v8
	v_mov_b32_e32 v198, v174
	v_mov_b32_e32 v189, v190
	v_mov_b32_e32 v37, v36
	v_mov_b32_e32 v38, v36
	v_mov_b32_e32 v39, v36
	v_mov_b32_e32 v40, v36
	v_mov_b32_e32 v41, v36
	v_mov_b32_e32 v42, v36
	v_mov_b32_e32 v43, v36
	v_mov_b32_e32 v44, v36
	v_mov_b32_e32 v45, v36
	v_mov_b32_e32 v46, v36
	v_mov_b32_e32 v47, v36
	v_mov_b32_e32 v48, v36
	v_mov_b32_e32 v49, v36
	v_mov_b32_e32 v50, v36
	v_mov_b32_e32 v51, v36
	v_mov_b32_e32 v52, v36
	v_mov_b32_e32 v53, v36
	v_mov_b32_e32 v54, v36
	v_mov_b32_e32 v55, v36
	v_mov_b32_e32 v56, v36
	v_mov_b32_e32 v57, v36
	v_mov_b32_e32 v58, v36
	v_mov_b32_e32 v59, v36
	v_mov_b32_e32 v60, v36
	v_mov_b32_e32 v61, v36
	v_mov_b32_e32 v62, v36
	v_mov_b32_e32 v63, v36
	v_mov_b32_e32 v64, v36
	v_mov_b32_e32 v65, v36
	v_mov_b32_e32 v66, v36
	v_mov_b32_e32 v67, v36
	v_mov_b32_e32 v68, v36
	v_mov_b32_e32 v69, v36
	v_mov_b32_e32 v70, v36
	v_mov_b32_e32 v71, v36
	v_mov_b32_e32 v72, v36
	v_mov_b32_e32 v73, v36
	v_mov_b32_e32 v74, v36
	v_mov_b32_e32 v75, v36
	v_mov_b32_e32 v76, v36
	v_mov_b32_e32 v77, v36
	v_mov_b32_e32 v78, v36
	v_mov_b32_e32 v79, v36
	v_mov_b32_e32 v80, v36
	v_mov_b32_e32 v81, v36
	v_mov_b32_e32 v82, v36
	v_mov_b32_e32 v83, v36
	v_mov_b32_e32 v84, v36
	v_mov_b32_e32 v85, v36
	v_mov_b32_e32 v86, v36
	v_mov_b32_e32 v87, v36
	v_mov_b32_e32 v88, v36
	v_mov_b32_e32 v89, v36
	v_mov_b32_e32 v90, v36
	v_mov_b32_e32 v91, v36
	v_mov_b32_e32 v92, v36
	v_mov_b32_e32 v93, v36
	v_mov_b32_e32 v94, v36
	v_mov_b32_e32 v95, v36
	v_mov_b32_e32 v96, v36
	v_mov_b32_e32 v97, v36
	v_mov_b32_e32 v98, v36
	v_mov_b32_e32 v99, v36
	v_mov_b32_e32 v100, v36
	v_mov_b32_e32 v101, v36
	v_mov_b32_e32 v102, v36
	v_mov_b32_e32 v103, v36
	v_mov_b32_e32 v104, v36
	v_mov_b32_e32 v105, v36
	v_mov_b32_e32 v106, v36
	v_mov_b32_e32 v107, v36
	v_mov_b32_e32 v108, v36
	v_mov_b32_e32 v109, v36
	v_mov_b32_e32 v110, v36
	v_mov_b32_e32 v111, v36
	v_mov_b32_e32 v112, v36
	v_mov_b32_e32 v113, v36
	v_mov_b32_e32 v114, v36
	v_mov_b32_e32 v115, v36
	v_mov_b32_e32 v116, v36
	v_mov_b32_e32 v117, v36
	v_mov_b32_e32 v118, v36
	v_mov_b32_e32 v119, v36
	v_mov_b32_e32 v120, v36
	v_mov_b32_e32 v121, v36
	v_mov_b32_e32 v122, v36
	v_mov_b32_e32 v123, v36
	v_mov_b32_e32 v124, v36
	v_mov_b32_e32 v125, v36
	v_mov_b32_e32 v126, v36
	v_mov_b32_e32 v127, v36
	v_mov_b32_e32 v128, v36
	v_mov_b32_e32 v129, v36
	v_mov_b32_e32 v130, v36
	v_mov_b32_e32 v131, v36
	v_mov_b32_e32 v132, v36
	v_mov_b32_e32 v133, v36
	v_mov_b32_e32 v134, v36
	v_mov_b32_e32 v135, v36
	v_mov_b32_e32 v136, v36
	v_mov_b32_e32 v137, v36
	v_mov_b32_e32 v138, v36
	v_mov_b32_e32 v139, v36
	v_mov_b32_e32 v140, v36
	v_mov_b32_e32 v141, v36
	v_mov_b32_e32 v142, v36
	v_mov_b32_e32 v143, v36
	v_mov_b32_e32 v144, v36
	v_mov_b32_e32 v145, v36
	v_mov_b32_e32 v146, v36
	v_mov_b32_e32 v147, v36
	v_mov_b32_e32 v148, v36
	v_mov_b32_e32 v149, v36
	v_mov_b32_e32 v150, v36
	v_mov_b32_e32 v151, v36
	v_mov_b32_e32 v152, v36
	v_mov_b32_e32 v153, v36
	v_mov_b32_e32 v154, v36
	v_mov_b32_e32 v155, v36
	v_mov_b32_e32 v156, v36
	v_mov_b32_e32 v157, v36
	v_mov_b32_e32 v158, v36
	v_mov_b32_e32 v159, v36
	v_mov_b32_e32 v160, v36
	v_mov_b32_e32 v161, v36
	v_mov_b32_e32 v162, v36
	v_mov_b32_e32 v163, v36
	s_barrier
	s_branch .LBB0_811

.LBB0_888:
	s_ashr_i32 s17, s16, 31
	v_mov_b32_e32 v173, v35
	s_lshl_b64 s[30:31], s[16:17], 19
	v_readlane_b32 s26, v253, 53
	v_lshl_add_u64 v[16:17], v[196:197], 0, v[172:173]
	v_mov_b32_e32 v169, v35
	v_readlane_b32 s27, v253, 54
	s_add_u32 s30, s26, s30
	v_lshl_add_u64 v[18:19], v[196:197], 0, v[168:169]
	s_addc_u32 s31, s27, s31
	s_add_i32 m0, s72, 0x18000
	v_lshl_add_u64 v[16:17], v[16:17], 0, s[18:19]
	global_load_lds_dwordx4 v[16:17], off
	v_lshl_add_u64 v[16:17], v[18:19], 0, s[18:19]
	s_add_i32 m0, s72, 0x1a000
	s_add_i32 s77, s72, 0x8000
	global_load_lds_dwordx4 v[16:17], off
	v_lshl_add_u64 v[2:3], v[2:3], 0, s[18:19]
	s_mov_b32 m0, s77
	s_add_i32 s78, s72, 0xa000
	global_load_lds_dwordx4 v[2:3], off
	v_lshl_add_u64 v[2:3], v[4:5], 0, s[18:19]
	s_mov_b32 m0, s78
	v_bfe_u32 v165, v10, 4, 2
	global_load_lds_dwordx4 v[2:3], off
	v_lshl_add_u64 v[2:3], v[196:197], 0, s[34:35]
	s_add_i32 m0, s72, 0x1c000
	v_lshl_add_u64 v[4:5], v[2:3], 0, v[172:173]
	global_load_lds_dwordx4 v[4:5], off
	v_lshl_add_u64 v[2:3], v[2:3], 0, v[168:169]
	s_add_i32 m0, s72, 0x1e000
	v_and_b32_e32 v1, 15, v10
	global_load_lds_dwordx4 v[2:3], off
	v_lshlrev_b32_e32 v15, 4, v165
	v_lshlrev_b32_e32 v10, 2, v10
	s_lshl_b32 s17, s6, 6
	v_lshl_or_b32 v15, v1, 6, v15
	s_lshl_b32 s6, s6, 13
	v_and_b32_e32 v10, 32, v10
	s_lshl_b32 s5, s5, 5
	v_bitop3_b32 v20, v15, s6, v10 bitop3:0xde
	s_and_b32 s76, s5, 0x60
	s_movk_i32 s6, 0x700
	s_lshl_b32 s5, s76, 7
	v_lshrrev_b32_e32 v3, 1, v12
	v_mul_lo_u32 v2, v11, s6
	s_movk_i32 s7, 0x7000
	v_bitop3_b32 v167, v15, s5, v10 bitop3:0xde
	s_cmpk_lt_u32 s4, 0x100
	v_mad_u64_u32 v[2:3], s[4:5], v3, s7, v[2:3]
	v_or_b32_e32 v2, v2, v13
	v_add_lshl_u32 v34, v2, v14, 1
	v_lshrrev_b32_e32 v3, 1, v6
	v_mul_lo_u32 v2, v7, s6
	v_mad_u64_u32 v[2:3], s[4:5], v3, s7, v[2:3]
	s_waitcnt vmcnt(8)
	s_barrier
	s_waitcnt vmcnt(6)
	s_mov_b64 s[24:25], 0x70180
	v_or_b32_e32 v2, v2, v8
	v_lshl_add_u64 v[190:191], v[34:35], 0, s[24:25]
	v_add_lshl_u32 v34, v2, v9, 1
	v_mov_b32_e32 v36, 0
	s_cselect_b64 s[36:37], -1, 0
	s_mov_b64 s[26:27], 0x70180
	v_lshl_add_u64 v[192:193], v[34:35], 0, s[24:25]
	s_mov_b32 s79, 0
	v_add_u32_e32 v189, 0, v20
	v_mov_b32_e32 v37, v36
	v_mov_b32_e32 v38, v36
	v_mov_b32_e32 v39, v36
	v_mov_b32_e32 v40, v36
	v_mov_b32_e32 v41, v36
	v_mov_b32_e32 v42, v36
	v_mov_b32_e32 v43, v36
	v_mov_b32_e32 v44, v36
	v_mov_b32_e32 v45, v36
	v_mov_b32_e32 v46, v36
	v_mov_b32_e32 v47, v36
	v_mov_b32_e32 v48, v36
	v_mov_b32_e32 v49, v36
	v_mov_b32_e32 v50, v36
	v_mov_b32_e32 v51, v36
	v_mov_b32_e32 v52, v36
	v_mov_b32_e32 v53, v36
	v_mov_b32_e32 v54, v36
	v_mov_b32_e32 v55, v36
	v_mov_b32_e32 v56, v36
	v_mov_b32_e32 v57, v36
	v_mov_b32_e32 v58, v36
	v_mov_b32_e32 v59, v36
	v_mov_b32_e32 v60, v36
	v_mov_b32_e32 v61, v36
	v_mov_b32_e32 v62, v36
	v_mov_b32_e32 v63, v36
	v_mov_b32_e32 v64, v36
	v_mov_b32_e32 v65, v36
	v_mov_b32_e32 v66, v36
	v_mov_b32_e32 v67, v36
	v_mov_b32_e32 v68, v36
	v_mov_b32_e32 v69, v36
	v_mov_b32_e32 v70, v36
	v_mov_b32_e32 v71, v36
	v_mov_b32_e32 v72, v36
	v_mov_b32_e32 v73, v36
	v_mov_b32_e32 v74, v36
	v_mov_b32_e32 v75, v36
	v_mov_b32_e32 v76, v36
	v_mov_b32_e32 v77, v36
	v_mov_b32_e32 v78, v36
	v_mov_b32_e32 v79, v36
	v_mov_b32_e32 v80, v36
	v_mov_b32_e32 v81, v36
	v_mov_b32_e32 v82, v36
	v_mov_b32_e32 v83, v36
	v_mov_b32_e32 v84, v36
	v_mov_b32_e32 v85, v36
	v_mov_b32_e32 v86, v36
	v_mov_b32_e32 v87, v36
	v_mov_b32_e32 v88, v36
	v_mov_b32_e32 v89, v36
	v_mov_b32_e32 v90, v36
	v_mov_b32_e32 v91, v36
	v_mov_b32_e32 v92, v36
	v_mov_b32_e32 v93, v36
	v_mov_b32_e32 v94, v36
	v_mov_b32_e32 v95, v36
	v_mov_b32_e32 v96, v36
	v_mov_b32_e32 v97, v36
	v_mov_b32_e32 v98, v36
	v_mov_b32_e32 v99, v36
	v_mov_b32_e32 v100, v36
	v_mov_b32_e32 v101, v36
	v_mov_b32_e32 v102, v36
	v_mov_b32_e32 v103, v36
	v_mov_b32_e32 v104, v36
	v_mov_b32_e32 v105, v36
	v_mov_b32_e32 v106, v36
	v_mov_b32_e32 v107, v36
	v_mov_b32_e32 v108, v36
	v_mov_b32_e32 v109, v36
	v_mov_b32_e32 v110, v36
	v_mov_b32_e32 v111, v36
	v_mov_b32_e32 v112, v36
	v_mov_b32_e32 v113, v36
	v_mov_b32_e32 v114, v36
	v_mov_b32_e32 v115, v36
	v_mov_b32_e32 v116, v36
	v_mov_b32_e32 v117, v36
	v_mov_b32_e32 v118, v36
	v_mov_b32_e32 v119, v36
	v_mov_b32_e32 v120, v36
	v_mov_b32_e32 v121, v36
	v_mov_b32_e32 v122, v36
	v_mov_b32_e32 v123, v36
	v_mov_b32_e32 v124, v36
	v_mov_b32_e32 v125, v36
	v_mov_b32_e32 v126, v36
	v_mov_b32_e32 v127, v36
	v_mov_b32_e32 v128, v36
	v_mov_b32_e32 v129, v36
	v_mov_b32_e32 v130, v36
	v_mov_b32_e32 v131, v36
	v_mov_b32_e32 v132, v36
	v_mov_b32_e32 v133, v36
	v_mov_b32_e32 v134, v36
	v_mov_b32_e32 v135, v36
	v_mov_b32_e32 v136, v36
	v_mov_b32_e32 v137, v36
	v_mov_b32_e32 v138, v36
	v_mov_b32_e32 v139, v36
	v_mov_b32_e32 v140, v36
	v_mov_b32_e32 v141, v36
	v_mov_b32_e32 v142, v36
	v_mov_b32_e32 v143, v36
	v_mov_b32_e32 v144, v36
	v_mov_b32_e32 v145, v36
	v_mov_b32_e32 v146, v36
	v_mov_b32_e32 v147, v36
	v_mov_b32_e32 v148, v36
	v_mov_b32_e32 v149, v36
	v_mov_b32_e32 v150, v36
	v_mov_b32_e32 v151, v36
	v_mov_b32_e32 v152, v36
	v_mov_b32_e32 v153, v36
	v_mov_b32_e32 v154, v36
	v_mov_b32_e32 v155, v36
	v_mov_b32_e32 v156, v36
	v_mov_b32_e32 v157, v36
	v_mov_b32_e32 v158, v36
	v_mov_b32_e32 v159, v36
	v_mov_b32_e32 v160, v36
	v_mov_b32_e32 v161, v36
	v_mov_b32_e32 v162, v36
	v_mov_b32_e32 v163, v36
	s_barrier
	s_branch .LBB0_891

.LBB0_934:
	s_bitcmp1_b32 s47, 0
	s_cselect_b32 s14, 0x7700000, 0
	v_readlane_b32 s22, v253, 26
	v_bfe_u32 v165, v168, 4, 2
	v_readlane_b32 s23, v253, 27
	s_add_u32 s22, s22, s14
	v_and_b32_e32 v1, 15, v168
	v_lshlrev_b32_e32 v6, 4, v165
	v_lshlrev_b32_e32 v7, 2, v168
	s_addc_u32 s23, s23, 0
	v_lshl_or_b32 v6, v1, 6, v6
	s_lshl_b32 s14, s36, 13
	v_and_b32_e32 v7, 32, v7
	v_bitop3_b32 v8, v6, s14, v7 bitop3:0xde
	s_lshl_b32 s14, s37, 5
	s_and_b32 s89, s14, 0x60
	s_add_i32 m0, s52, 0x18000
	v_lshl_add_u64 v[4:5], v[4:5], 0, s[18:19]
	v_readlane_b32 s26, v253, 28
	s_lshl_b32 s87, s36, 6
	s_lshl_b32 s14, s89, 7
	global_load_lds_dwordx4 v[4:5], off
	v_lshl_add_u64 v[2:3], v[2:3], 0, s[18:19]
	s_add_i32 m0, s52, 0x1a000
	v_readlane_b32 s27, v253, 29
	s_add_i32 s90, s52, 0x8000
	s_add_i32 s91, s52, 0xa000
	v_mov_b32_e32 v193, v35
	global_load_lds_dwordx4 v[2:3], off
	v_lshl_add_u64 v[2:3], s[26:27], 0, v[34:35]
	s_mov_b32 m0, s90
	s_add_u32 s36, s30, 0x20080
	global_load_lds_dwordx4 v[2:3], off
	v_lshl_add_u64 v[2:3], s[26:27], 0, v[192:193]
	s_mov_b32 m0, s91
	s_addc_u32 s37, s31, 0
	global_load_lds_dwordx4 v[2:3], off
	s_add_i32 m0, s52, 0x1c000
	v_lshl_add_u64 v[2:3], s[36:37], 0, v[170:171]
	global_load_lds_dwordx4 v[2:3], off
	v_lshl_add_u64 v[2:3], s[36:37], 0, v[172:173]
	s_add_i32 m0, s52, 0x1e000
	v_mov_b32_e32 v36, 0
	global_load_lds_dwordx4 v[2:3], off
	s_waitcnt vmcnt(8)
	s_barrier
	s_waitcnt vmcnt(6)
	s_cmpk_lt_u32 s46, 0x100
	s_mov_b32 s88, 0
	v_bitop3_b32 v167, v6, s14, v7 bitop3:0xde
	s_cselect_b64 s[36:37], -1, 0
	v_add_u32_e32 v169, 0, v8
	v_mov_b32_e32 v198, v174
	v_mov_b32_e32 v189, v190
	v_mov_b32_e32 v37, v36
	v_mov_b32_e32 v38, v36
	v_mov_b32_e32 v39, v36
	v_mov_b32_e32 v40, v36
	v_mov_b32_e32 v41, v36
	v_mov_b32_e32 v42, v36
	v_mov_b32_e32 v43, v36
	v_mov_b32_e32 v44, v36
	v_mov_b32_e32 v45, v36
	v_mov_b32_e32 v46, v36
	v_mov_b32_e32 v47, v36
	v_mov_b32_e32 v48, v36
	v_mov_b32_e32 v49, v36
	v_mov_b32_e32 v50, v36
	v_mov_b32_e32 v51, v36
	v_mov_b32_e32 v52, v36
	v_mov_b32_e32 v53, v36
	v_mov_b32_e32 v54, v36
	v_mov_b32_e32 v55, v36
	v_mov_b32_e32 v56, v36
	v_mov_b32_e32 v57, v36
	v_mov_b32_e32 v58, v36
	v_mov_b32_e32 v59, v36
	v_mov_b32_e32 v60, v36
	v_mov_b32_e32 v61, v36
	v_mov_b32_e32 v62, v36
	v_mov_b32_e32 v63, v36
	v_mov_b32_e32 v64, v36
	v_mov_b32_e32 v65, v36
	v_mov_b32_e32 v66, v36
	v_mov_b32_e32 v67, v36
	v_mov_b32_e32 v68, v36
	v_mov_b32_e32 v69, v36
	v_mov_b32_e32 v70, v36
	v_mov_b32_e32 v71, v36
	v_mov_b32_e32 v72, v36
	v_mov_b32_e32 v73, v36
	v_mov_b32_e32 v74, v36
	v_mov_b32_e32 v75, v36
	v_mov_b32_e32 v76, v36
	v_mov_b32_e32 v77, v36
	v_mov_b32_e32 v78, v36
	v_mov_b32_e32 v79, v36
	v_mov_b32_e32 v80, v36
	v_mov_b32_e32 v81, v36
	v_mov_b32_e32 v82, v36
	v_mov_b32_e32 v83, v36
	v_mov_b32_e32 v84, v36
	v_mov_b32_e32 v85, v36
	v_mov_b32_e32 v86, v36
	v_mov_b32_e32 v87, v36
	v_mov_b32_e32 v88, v36
	v_mov_b32_e32 v89, v36
	v_mov_b32_e32 v90, v36
	v_mov_b32_e32 v91, v36
	v_mov_b32_e32 v92, v36
	v_mov_b32_e32 v93, v36
	v_mov_b32_e32 v94, v36
	v_mov_b32_e32 v95, v36
	v_mov_b32_e32 v96, v36
	v_mov_b32_e32 v97, v36
	v_mov_b32_e32 v98, v36
	v_mov_b32_e32 v99, v36
	v_mov_b32_e32 v100, v36
	v_mov_b32_e32 v101, v36
	v_mov_b32_e32 v102, v36
	v_mov_b32_e32 v103, v36
	v_mov_b32_e32 v104, v36
	v_mov_b32_e32 v105, v36
	v_mov_b32_e32 v106, v36
	v_mov_b32_e32 v107, v36
	v_mov_b32_e32 v108, v36
	v_mov_b32_e32 v109, v36
	v_mov_b32_e32 v110, v36
	v_mov_b32_e32 v111, v36
	v_mov_b32_e32 v112, v36
	v_mov_b32_e32 v113, v36
	v_mov_b32_e32 v114, v36
	v_mov_b32_e32 v115, v36
	v_mov_b32_e32 v116, v36
	v_mov_b32_e32 v117, v36
	v_mov_b32_e32 v118, v36
	v_mov_b32_e32 v119, v36
	v_mov_b32_e32 v120, v36
	v_mov_b32_e32 v121, v36
	v_mov_b32_e32 v122, v36
	v_mov_b32_e32 v123, v36
	v_mov_b32_e32 v124, v36
	v_mov_b32_e32 v125, v36
	v_mov_b32_e32 v126, v36
	v_mov_b32_e32 v127, v36
	v_mov_b32_e32 v128, v36
	v_mov_b32_e32 v129, v36
	v_mov_b32_e32 v130, v36
	v_mov_b32_e32 v131, v36
	v_mov_b32_e32 v132, v36
	v_mov_b32_e32 v133, v36
	v_mov_b32_e32 v134, v36
	v_mov_b32_e32 v135, v36
	v_mov_b32_e32 v136, v36
	v_mov_b32_e32 v137, v36
	v_mov_b32_e32 v138, v36
	v_mov_b32_e32 v139, v36
	v_mov_b32_e32 v140, v36
	v_mov_b32_e32 v141, v36
	v_mov_b32_e32 v142, v36
	v_mov_b32_e32 v143, v36
	v_mov_b32_e32 v144, v36
	v_mov_b32_e32 v145, v36
	v_mov_b32_e32 v146, v36
	v_mov_b32_e32 v147, v36
	v_mov_b32_e32 v148, v36
	v_mov_b32_e32 v149, v36
	v_mov_b32_e32 v150, v36
	v_mov_b32_e32 v151, v36
	v_mov_b32_e32 v152, v36
	v_mov_b32_e32 v153, v36
	v_mov_b32_e32 v154, v36
	v_mov_b32_e32 v155, v36
	v_mov_b32_e32 v156, v36
	v_mov_b32_e32 v157, v36
	v_mov_b32_e32 v158, v36
	v_mov_b32_e32 v159, v36
	v_mov_b32_e32 v160, v36
	v_mov_b32_e32 v161, v36
	v_mov_b32_e32 v162, v36
	v_mov_b32_e32 v163, v36
	s_barrier
	s_branch .LBB0_936

.LBB0_1081:
	v_lshl_add_u64 v[10:11], s[22:23], 0, v[34:35]
	v_mov_b32_e32 v165, v35
	v_readlane_b32 s30, v253, 62
	v_bfe_u32 v189, v5, 4, 2
	s_lshl_b32 s5, s5, 5
	v_lshl_add_u64 v[12:13], s[22:23], 0, v[164:165]
	v_mov_b32_e32 v169, v35
	v_readlane_b32 s31, v253, 63
	v_and_b32_e32 v1, 15, v5
	v_lshlrev_b32_e32 v9, 4, v189
	v_lshlrev_b32_e32 v5, 2, v5
	s_and_b32 s46, s5, 0x60
	s_add_i32 m0, s41, 0x18000
	v_lshl_add_u64 v[10:11], v[10:11], 0, s[18:19]
	v_lshl_add_u64 v[14:15], s[30:31], 0, v[168:169]
	v_mov_b32_e32 v167, v35
	s_lshl_b32 s45, s8, 6
	v_lshl_or_b32 v9, v1, 6, v9
	s_lshl_b32 s8, s8, 13
	v_and_b32_e32 v5, 32, v5
	s_lshl_b32 s5, s46, 7
	global_load_lds_dwordx4 v[10:11], off
	v_lshl_add_u64 v[10:11], v[12:13], 0, s[18:19]
	s_add_i32 m0, s41, 0x1a000
	s_add_i32 s47, s41, 0x8000
	s_add_i32 s48, s41, 0xa000
	v_lshl_add_u64 v[16:17], s[30:31], 0, v[166:167]
	v_bitop3_b32 v18, v9, s8, v5 bitop3:0xde
	global_load_lds_dwordx4 v[10:11], off
	v_lshl_add_u64 v[10:11], v[14:15], 0, s[18:19]
	s_mov_b32 m0, s47
	s_add_u32 s8, s22, 0x20080
	global_load_lds_dwordx4 v[10:11], off
	v_lshl_add_u64 v[10:11], v[16:17], 0, s[18:19]
	s_mov_b32 m0, s48
	s_addc_u32 s9, s23, 0
	global_load_lds_dwordx4 v[10:11], off
	s_add_i32 m0, s41, 0x1c000
	v_lshl_add_u64 v[10:11], s[8:9], 0, v[34:35]
	global_load_lds_dwordx4 v[10:11], off
	v_lshl_add_u64 v[10:11], s[8:9], 0, v[164:165]
	s_add_i32 m0, s41, 0x1e000
	v_bitop3_b32 v196, v9, s5, v5 bitop3:0xde
	global_load_lds_dwordx4 v[10:11], off
	v_lshlrev_b32_e32 v5, 13, v7
	v_and_b32_e32 v5, 0xffffc000, v5
	v_lshl_add_u32 v5, v6, 10, v5
	v_and_b32_e32 v6, 1, v7
	v_lshl_or_b32 v5, v6, 6, v5
	v_lshl_add_u32 v170, v8, 1, v5
	v_lshlrev_b32_e32 v5, 13, v2
	v_and_b32_e32 v5, 0xffffc000, v5
	s_waitcnt vmcnt(8)
	s_barrier
	s_waitcnt vmcnt(6)
	v_lshl_add_u32 v3, v3, 10, v5
	v_and_b32_e32 v2, 1, v2
	s_cmpk_lt_u32 s4, 0x100
	v_lshl_or_b32 v2, v2, 6, v3
	v_mov_b32_e32 v36, 0
	s_cselect_b64 s[8:9], -1, 0
	v_mov_b32_e32 v171, v35
	v_lshl_add_u32 v172, v4, 1, v2
	v_mov_b32_e32 v173, v35
	s_mov_b32 s49, 0
	v_add_u32_e32 v197, 0, v18
	v_readlane_b32 s52, v253, 60
	v_readlane_b32 s53, v253, 59
	v_mov_b32_e32 v37, v36
	v_mov_b32_e32 v38, v36
	v_mov_b32_e32 v39, v36
	v_mov_b32_e32 v40, v36
	v_mov_b32_e32 v41, v36
	v_mov_b32_e32 v42, v36
	v_mov_b32_e32 v43, v36
	v_mov_b32_e32 v44, v36
	v_mov_b32_e32 v45, v36
	v_mov_b32_e32 v46, v36
	v_mov_b32_e32 v47, v36
	v_mov_b32_e32 v48, v36
	v_mov_b32_e32 v49, v36
	v_mov_b32_e32 v50, v36
	v_mov_b32_e32 v51, v36
	v_mov_b32_e32 v52, v36
	v_mov_b32_e32 v53, v36
	v_mov_b32_e32 v54, v36
	v_mov_b32_e32 v55, v36
	v_mov_b32_e32 v56, v36
	v_mov_b32_e32 v57, v36
	v_mov_b32_e32 v58, v36
	v_mov_b32_e32 v59, v36
	v_mov_b32_e32 v60, v36
	v_mov_b32_e32 v61, v36
	v_mov_b32_e32 v62, v36
	v_mov_b32_e32 v63, v36
	v_mov_b32_e32 v64, v36
	v_mov_b32_e32 v65, v36
	v_mov_b32_e32 v66, v36
	v_mov_b32_e32 v67, v36
	v_mov_b32_e32 v68, v36
	v_mov_b32_e32 v69, v36
	v_mov_b32_e32 v70, v36
	v_mov_b32_e32 v71, v36
	v_mov_b32_e32 v72, v36
	v_mov_b32_e32 v73, v36
	v_mov_b32_e32 v74, v36
	v_mov_b32_e32 v75, v36
	v_mov_b32_e32 v76, v36
	v_mov_b32_e32 v77, v36
	v_mov_b32_e32 v78, v36
	v_mov_b32_e32 v79, v36
	v_mov_b32_e32 v80, v36
	v_mov_b32_e32 v81, v36
	v_mov_b32_e32 v82, v36
	v_mov_b32_e32 v83, v36
	v_mov_b32_e32 v84, v36
	v_mov_b32_e32 v85, v36
	v_mov_b32_e32 v86, v36
	v_mov_b32_e32 v87, v36
	v_mov_b32_e32 v88, v36
	v_mov_b32_e32 v89, v36
	v_mov_b32_e32 v90, v36
	v_mov_b32_e32 v91, v36
	v_mov_b32_e32 v92, v36
	v_mov_b32_e32 v93, v36
	v_mov_b32_e32 v94, v36
	v_mov_b32_e32 v95, v36
	v_mov_b32_e32 v96, v36
	v_mov_b32_e32 v97, v36
	v_mov_b32_e32 v98, v36
	v_mov_b32_e32 v99, v36
	v_mov_b32_e32 v100, v36
	v_mov_b32_e32 v101, v36
	v_mov_b32_e32 v102, v36
	v_mov_b32_e32 v103, v36
	v_mov_b32_e32 v104, v36
	v_mov_b32_e32 v105, v36
	v_mov_b32_e32 v106, v36
	v_mov_b32_e32 v107, v36
	v_mov_b32_e32 v108, v36
	v_mov_b32_e32 v109, v36
	v_mov_b32_e32 v110, v36
	v_mov_b32_e32 v111, v36
	v_mov_b32_e32 v112, v36
	v_mov_b32_e32 v113, v36
	v_mov_b32_e32 v114, v36
	v_mov_b32_e32 v115, v36
	v_mov_b32_e32 v116, v36
	v_mov_b32_e32 v117, v36
	v_mov_b32_e32 v118, v36
	v_mov_b32_e32 v119, v36
	v_mov_b32_e32 v120, v36
	v_mov_b32_e32 v121, v36
	v_mov_b32_e32 v122, v36
	v_mov_b32_e32 v123, v36
	v_mov_b32_e32 v124, v36
	v_mov_b32_e32 v125, v36
	v_mov_b32_e32 v126, v36
	v_mov_b32_e32 v127, v36
	v_mov_b32_e32 v128, v36
	v_mov_b32_e32 v129, v36
	v_mov_b32_e32 v130, v36
	v_mov_b32_e32 v131, v36
	v_mov_b32_e32 v132, v36
	v_mov_b32_e32 v133, v36
	v_mov_b32_e32 v134, v36
	v_mov_b32_e32 v135, v36
	v_mov_b32_e32 v136, v36
	v_mov_b32_e32 v137, v36
	v_mov_b32_e32 v138, v36
	v_mov_b32_e32 v139, v36
	v_mov_b32_e32 v140, v36
	v_mov_b32_e32 v141, v36
	v_mov_b32_e32 v142, v36
	v_mov_b32_e32 v143, v36
	v_mov_b32_e32 v144, v36
	v_mov_b32_e32 v145, v36
	v_mov_b32_e32 v146, v36
	v_mov_b32_e32 v147, v36
	v_mov_b32_e32 v148, v36
	v_mov_b32_e32 v149, v36
	v_mov_b32_e32 v150, v36
	v_mov_b32_e32 v151, v36
	v_mov_b32_e32 v152, v36
	v_mov_b32_e32 v153, v36
	v_mov_b32_e32 v154, v36
	v_mov_b32_e32 v155, v36
	v_mov_b32_e32 v156, v36
	v_mov_b32_e32 v157, v36
	v_mov_b32_e32 v158, v36
	v_mov_b32_e32 v159, v36
	v_mov_b32_e32 v160, v36
	v_mov_b32_e32 v161, v36
	v_mov_b32_e32 v162, v36
	v_mov_b32_e32 v163, v36
	s_barrier
	s_branch .LBB0_1084

.LBB0_1150:
	v_readlane_b32 s9, v255, 11
	s_add_u32 s47, s9, 0x5000
	v_readlane_b32 s9, v255, 12
	v_readlane_b32 s30, v254, 6
	s_addc_u32 s48, s9, 0
	v_bfe_u32 v189, v14, 4, 2
	s_lshl_b32 s5, s5, 5
	v_mov_b32_e32 v169, v35
	v_readlane_b32 s31, v254, 7
	v_and_b32_e32 v1, 15, v14
	v_lshlrev_b32_e32 v15, 4, v189
	v_lshlrev_b32_e32 v14, 2, v14
	s_and_b32 s50, s5, 0x60
	s_add_i32 m0, s43, 0x18000
	v_lshl_add_u64 v[2:3], v[2:3], 0, s[18:19]
	v_lshl_add_u64 v[16:17], s[30:31], 0, v[168:169]
	v_mov_b32_e32 v167, v35
	s_lshl_b32 s49, s8, 6
	v_lshl_or_b32 v15, v1, 6, v15
	s_lshl_b32 s8, s8, 13
	v_and_b32_e32 v14, 32, v14
	s_lshl_b32 s5, s50, 7
	global_load_lds_dwordx4 v[2:3], off
	v_lshl_add_u64 v[2:3], v[4:5], 0, s[18:19]
	s_add_i32 m0, s43, 0x1a000
	s_add_i32 s51, s43, 0x8000
	s_add_i32 s52, s43, 0xa000
	v_lshl_add_u64 v[18:19], s[30:31], 0, v[166:167]
	v_bitop3_b32 v20, v15, s8, v14 bitop3:0xde
	global_load_lds_dwordx4 v[2:3], off
	v_lshl_add_u64 v[2:3], v[16:17], 0, s[18:19]
	s_mov_b32 m0, s51
	s_add_u32 s8, s22, 0x58080
	global_load_lds_dwordx4 v[2:3], off
	v_lshl_add_u64 v[2:3], v[18:19], 0, s[18:19]
	s_mov_b32 m0, s52
	s_addc_u32 s9, s23, 0
	global_load_lds_dwordx4 v[2:3], off
	s_add_i32 m0, s43, 0x1c000
	v_lshl_add_u64 v[2:3], s[8:9], 0, v[34:35]
	global_load_lds_dwordx4 v[2:3], off
	v_lshl_add_u64 v[2:3], s[8:9], 0, v[164:165]
	s_add_i32 m0, s43, 0x1e000
	s_movk_i32 s10, 0x580
	global_load_lds_dwordx4 v[2:3], off
	v_lshrrev_b32_e32 v3, 1, v11
	v_mul_lo_u32 v2, v10, s10
	s_movk_i32 s11, 0x5800
	v_bitop3_b32 v222, v15, s5, v14 bitop3:0xde
	s_cmpk_lt_u32 s4, 0x100
	v_mad_u64_u32 v[2:3], s[4:5], v3, s11, v[2:3]
	v_or_b32_e32 v2, v2, v12
	v_add_lshl_u32 v2, v2, v13, 1
	v_mov_b32_e32 v3, v35
	s_mov_b64 s[16:17], 0x58080
	v_lshl_add_u64 v[170:171], v[2:3], 0, s[16:17]
	v_lshrrev_b32_e32 v3, 1, v6
	v_mul_lo_u32 v2, v7, s10
	v_mad_u64_u32 v[2:3], s[4:5], v3, s11, v[2:3]
	s_waitcnt vmcnt(8)
	s_barrier
	s_waitcnt vmcnt(6)
	v_or_b32_e32 v2, v2, v8
	v_add_lshl_u32 v2, v2, v9, 1
	v_mov_b32_e32 v3, v35
	s_cselect_b64 s[8:9], -1, 0
	v_lshl_add_u64 v[172:173], v[2:3], 0, s[16:17]
	s_mov_b32 s53, 0
	v_add_u32_e32 v223, 0, v20
	v_readlane_b32 s57, v254, 2
	v_readlane_b32 s56, v254, 3
	s_barrier
	s_branch .LBB0_1153
